# speedup vs baseline: 1.0047x; 1.0047x over previous
.LBB0_8:
	s_or_b64 exec, exec, s[4:5]
	s_waitcnt lgkmcnt(1)
	v_add_u32_e32 v1, v7, v6
	v_add_u32_e32 v1, v1, v8
	v_add_u32_e32 v1, v1, v9
	s_waitcnt lgkmcnt(0)
	v_add_u32_e32 v1, v1, v2
	v_add_u32_e32 v1, v1, v3
	v_add_u32_e32 v1, v1, v4
	v_add_u32_e32 v226, v1, v5
	s_movk_i32 s3, 0x400
	v_cmp_gt_i32_e64 s[8:9], s3, v226
	s_movk_i32 s3, 0x3ff
	v_cmp_lt_i32_e32 vcc, s3, v226
	s_movk_i32 s3, 0x100
	v_cmp_gt_u32_e64 s[4:5], s3, v0
	s_movk_i32 s3, 0xff
	s_and_b32 s41, s23, 0xffff
	s_and_b32 s29, s29, 0xffff
	s_mov_b32 s43, 0x20000
	s_mov_b32 s42, 0x10000
	v_lshl_or_b32 v1, v227, 12, v232
	v_cmp_lt_u32_e64 s[6:7], s3, v0
	s_cbranch_vccz .LBB0_18
	s_and_saveexec_b64 s[10:11], s[6:7]
	s_xor_b64 s[10:11], exec, s[10:11]
	s_cbranch_execz .LBB0_13
	s_setprio 1
	v_lshlrev_b32_e32 v3, 4, v218
	v_lshlrev_b32_e32 v4, 4, v0
	s_movk_i32 s3, 0xc00
	v_and_b32_e32 v2, 6, v222
	v_and_or_b32 v181, v4, s3, v3
	s_add_i32 s3, s46, s33
	v_lshl_or_b32 v182, v2, 10, v3
	v_add3_u32 v2, s3, v216, v221
	v_lshl_or_b32 v2, v2, 9, v232
	v_add_u32_e32 v183, 0x30000, v2
	v_mov_b32_e32 v2, 0
	v_lshl_or_b32 v180, v219, 12, v3
	s_mov_b32 s3, -2
	s_brev_b32 s16, 16
	s_mov_b32 s17, 0x10000
	s_waitcnt vmcnt(13)
	v_mov_b32_e32 v167, v45
	v_mov_b32_e32 v166, v44
	v_mov_b32_e32 v165, v43
	v_mov_b32_e32 v164, v42
	v_mov_b32_e32 v155, v41
	v_mov_b32_e32 v154, v40
	v_mov_b32_e32 v153, v39
	v_mov_b32_e32 v152, v38
	v_mov_b32_e32 v151, v37
	v_mov_b32_e32 v150, v36
	v_mov_b32_e32 v149, v35
	v_mov_b32_e32 v148, v34
	s_waitcnt vmcnt(12)
	v_mov_b32_e32 v156, v96
	v_mov_b32_e32 v157, v97
	v_mov_b32_e32 v158, v98
	v_mov_b32_e32 v159, v99
	s_waitcnt vmcnt(11)
	v_mov_b32_e32 v160, v100
	v_mov_b32_e32 v161, v101
	v_mov_b32_e32 v162, v102
	v_mov_b32_e32 v163, v103
	s_waitcnt vmcnt(10)
	v_mov_b32_e32 v168, v104
	v_mov_b32_e32 v169, v105
	v_mov_b32_e32 v170, v106
	v_mov_b32_e32 v171, v107
	s_waitcnt vmcnt(9)
	v_mov_b32_e32 v172, v108
	v_mov_b32_e32 v173, v109
	v_mov_b32_e32 v174, v110
	v_mov_b32_e32 v175, v111
	s_waitcnt vmcnt(8)
	v_mov_b32_e32 v176, v112
	v_mov_b32_e32 v177, v113
	v_mov_b32_e32 v178, v114
	v_mov_b32_e32 v179, v115
	v_mov_b32_e32 v3, v2
	v_mov_b32_e32 v4, v2
	v_mov_b32_e32 v5, v2
	v_mov_b32_e32 v6, v2
	v_mov_b32_e32 v7, v2
	v_mov_b32_e32 v8, v2
	v_mov_b32_e32 v9, v2
	v_mov_b32_e32 v10, v2
	v_mov_b32_e32 v11, v2
	v_mov_b32_e32 v12, v2
	v_mov_b32_e32 v13, v2
	v_mov_b32_e32 v14, v2
	v_mov_b32_e32 v15, v2
	v_mov_b32_e32 v16, v2
	v_mov_b32_e32 v17, v2
	v_mov_b32_e32 v18, v2
	v_mov_b32_e32 v19, v2
	v_mov_b32_e32 v20, v2
	v_mov_b32_e32 v21, v2
	v_mov_b32_e32 v22, v2
	v_mov_b32_e32 v23, v2
	v_mov_b32_e32 v24, v2
	v_mov_b32_e32 v25, v2
	v_mov_b32_e32 v26, v2
	v_mov_b32_e32 v27, v2
	v_mov_b32_e32 v28, v2
	v_mov_b32_e32 v29, v2
	v_mov_b32_e32 v30, v2
	v_mov_b32_e32 v31, v2
	v_mov_b32_e32 v32, v2
	v_mov_b32_e32 v33, v2
